# speedup vs baseline: 1.0134x; 1.0047x over previous
_Z10ode_kernelPKfPKDF16_S2_PfPKi:
	v_lshrrev_b32_e32 v167, 6, v0
	s_lshr_b32 s3, s2, 3
	v_add_u32_e32 v2, s3, v167
	s_load_dwordx4 s[4:7], s[0:1], 0x0
	s_load_dwordx2 s[12:13], s[0:1], 0x10
	v_and_b32_e32 v130, 3, v2
	v_and_b32_e32 v1, 63, v0
	v_readfirstlane_b32 s3, v130
	v_lshlrev_b32_e32 v166, 4, v1
	s_lshl_b32 s11, s3, 14
	v_lshl_or_b32 v2, v130, 17, v166
	v_mov_b32_e32 v3, 0
	s_and_b32 s17, s11, 0xc000
	s_mov_b32 s9, 0
	s_waitcnt lgkmcnt(0)
	v_lshl_add_u64 v[74:75], s[6:7], 0, v[2:3]
	s_lshl_b32 s8, s17, 1
	v_lshl_add_u64 v[46:47], v[74:75], 0, s[8:9]
	s_movk_i32 s15, 0x1000
	v_add_co_u32_e32 v18, vcc, s15, v46
	s_movk_i32 s14, 0x3000
	s_nop 0
	v_addc_co_u32_e32 v19, vcc, 0, v47, vcc
	v_add_co_u32_e32 v20, vcc, s14, v46
	s_lshl_b32 s10, s2, 10
	s_nop 0
	v_addc_co_u32_e32 v21, vcc, 0, v47, vcc
	s_and_b32 s8, s10, 0x3e000
	s_movk_i32 s16, 0x7000
	v_add_co_u32_e32 v48, vcc, s16, v46
	v_lshl_or_b32 v22, v1, 7, s8
	s_add_i32 s8, s11, 0x4000
	v_addc_co_u32_e32 v49, vcc, 0, v47, vcc
	s_movk_i32 s16, 0x5000
	s_and_b32 s8, s8, 0xc000
	v_add_co_u32_e32 v50, vcc, s16, v46
	s_lshl_b32 s8, s8, 1
	global_load_dwordx4 v[34:37], v[18:19], off offset:2048
	global_load_dwordx4 v[14:17], v[20:21], off offset:2048
	global_load_dwordx4 v[6:9], v[20:21], off offset:1024
	global_load_dwordx4 v[2:5], v[18:19], off offset:1024
	global_load_dwordx4 v[42:45], v[18:19], off offset:3072
	global_load_dwordx4 v[38:41], v[20:21], off offset:3072
	v_addc_co_u32_e32 v51, vcc, 0, v47, vcc
	v_lshl_add_u64 v[72:73], v[74:75], 0, s[8:9]
	v_add_co_u32_e32 v106, vcc, s14, v72
	global_load_dwordx4 v[10:13], v[50:51], off offset:1024
	global_load_dwordx4 v[52:55], v[50:51], off offset:2048
	global_load_dwordx4 v[56:59], v[48:49], off offset:2048
	v_addc_co_u32_e32 v107, vcc, 0, v73, vcc
	v_add_co_u32_e32 v108, vcc, s15, v72
	global_load_dwordx4 v[60:63], v[50:51], off offset:3072
	global_load_dwordx4 v[64:67], v[48:49], off offset:3072
	global_load_ushort v198, v22, s[12:13]
	v_addc_co_u32_e32 v109, vcc, 0, v73, vcc
	global_load_dwordx4 v[68:71], v[108:109], off offset:2048
	global_load_dwordx4 v[78:81], v[106:107], off offset:2048
	global_load_dwordx4 v[82:85], v[106:107], off offset:3072
	global_load_dwordx4 v[86:89], v[108:109], off offset:3072
	s_add_i32 s8, s11, 0x6000
	s_movk_i32 s16, 0x2000
	s_and_b32 s8, s8, 0xe000
	v_add_co_u32_e32 v26, vcc, s16, v46
	s_lshl_b32 s8, s8, 1
	s_nop 0
	v_addc_co_u32_e32 v27, vcc, 0, v47, vcc
	v_lshl_add_u64 v[110:111], v[74:75], 0, s[8:9]
	v_add_co_u32_e32 v112, vcc, s14, v110
	global_load_dwordx4 a[0:3], v[46:47], off
	global_load_dwordx4 a[8:11], v[46:47], off offset:1024
	global_load_dwordx4 a[12:15], v[26:27], off offset:1024
	global_load_dwordx4 a[20:23], v[26:27], off offset:2048
	global_load_dwordx4 a[16:19], v[46:47], off offset:2048
	global_load_dwordx4 a[24:27], v[46:47], off offset:3072
	global_load_dwordx4 a[4:7], v[20:21], off offset:-4096
	global_load_dwordx4 v[22:25], v[20:21], off
	global_load_dwordx4 a[28:31], v[26:27], off offset:3072
	s_nop 0
	global_load_dwordx4 v[18:21], v[18:19], off
	v_addc_co_u32_e32 v113, vcc, 0, v111, vcc
	v_add_co_u32_e32 v114, vcc, s15, v110
	v_lshl_or_b32 v199, v167, 15, v166
	s_nop 0
	v_addc_co_u32_e32 v115, vcc, 0, v111, vcc
	global_load_dwordx4 v[26:29], v[114:115], off offset:1024
	global_load_dwordx4 v[90:93], v[114:115], off offset:2048
	global_load_dwordx4 v[30:33], v[112:113], off offset:1024
	global_load_dwordx4 v[94:97], v[112:113], off offset:2048
	global_load_dwordx4 v[98:101], v[114:115], off offset:3072
	global_load_dwordx4 v[102:105], v[112:113], off offset:3072
	s_movk_i32 s8, 0x6000
	s_load_dwordx2 s[6:7], s[0:1], 0x20
	v_lshlrev_b32_e32 v76, 1, v0
	v_and_b32_e32 v200, 7, v0
	v_and_b32_e32 v128, 64, v76
	v_and_b32_e32 v179, 15, v0
	v_bfe_u32 v201, v0, 4, 1
	v_mov_b32_e32 v196, 0x44444444
	global_load_dwordx4 a[44:47], v[48:49], off offset:-4096
	s_waitcnt vmcnt(31)
	ds_write_b128 v199, v[14:17] offset:1024
	v_add_co_u32_e32 v14, vcc, s8, v46
	s_movk_i32 s8, 0x4000
	s_nop 0
	v_addc_co_u32_e32 v15, vcc, 0, v47, vcc
	s_waitcnt vmcnt(28)
	ds_write_b128 v199, v[42:45] offset:2048
	v_add_co_u32_e32 v42, vcc, s8, v46
	ds_write_b128 v199, v[34:37]
	s_nop 0
	v_addc_co_u32_e32 v43, vcc, 0, v47, vcc
	s_waitcnt vmcnt(27)
	ds_write_b128 v199, v[38:41] offset:3072
	v_add_co_u32_e32 v44, vcc, s16, v72
	global_load_dwordx4 a[36:39], v[14:15], off offset:1024
	global_load_dwordx4 a[32:35], v[42:43], off offset:1024
	global_load_dwordx4 a[48:51], v[42:43], off offset:2048
	global_load_dwordx4 a[52:55], v[14:15], off offset:2048
	global_load_dwordx4 a[60:63], v[14:15], off offset:3072
	global_load_dwordx4 a[40:43], v[50:51], off offset:-4096
	global_load_dwordx4 v[34:37], v[50:51], off
	global_load_dwordx4 v[38:41], v[48:49], off
	s_nop 0
	global_load_dwordx4 v[14:17], v[48:49], off offset:1024
	s_waitcnt vmcnt(34)
	ds_write_b128 v199, v[52:55] offset:4096
	s_waitcnt vmcnt(33)
	ds_write_b128 v199, v[56:59] offset:5120
	v_addc_co_u32_e32 v45, vcc, 0, v73, vcc
	s_xor_b32 s8, s17, 0x8000
	global_load_dwordx4 a[68:71], v[106:107], off offset:-4096
	s_waitcnt vmcnt(33)
	ds_write_b128 v199, v[60:63] offset:6144
	s_waitcnt vmcnt(32)
	ds_write_b128 v199, v[64:67] offset:7168
	v_add_co_u32_e32 v58, vcc, s16, v110
	s_lshl_b32 s8, s8, 1
	global_load_dwordx4 a[56:59], v[42:43], off offset:3072
	global_load_dwordx4 a[64:67], v[72:73], off
	global_load_dwordx4 a[72:75], v[72:73], off offset:1024
	global_load_dwordx4 a[80:83], v[72:73], off offset:2048
	global_load_dwordx4 a[84:87], v[44:45], off offset:2048
	global_load_dwordx4 a[92:95], v[44:45], off offset:3072
	global_load_dwordx4 a[76:79], v[44:45], off offset:1024
	global_load_dwordx4 a[88:91], v[72:73], off offset:3072
	global_load_dwordx4 v[46:49], v[106:107], off
	global_load_dwordx4 v[54:57], v[106:107], off offset:1024
	s_nop 0
	global_load_dwordx4 v[42:45], v[108:109], off
	global_load_dwordx4 v[50:53], v[108:109], off offset:1024
	s_waitcnt vmcnt(42)
	ds_write_b128 v199, v[68:71] offset:8192
	s_waitcnt vmcnt(41)
	ds_write_b128 v199, v[78:81] offset:9216
	s_waitcnt vmcnt(39)
	ds_write_b128 v199, v[86:89] offset:10240
	ds_write_b128 v199, v[82:85] offset:11264
	v_addc_co_u32_e32 v59, vcc, 0, v111, vcc
	v_lshl_add_u64 v[78:79], v[74:75], 0, s[8:9]
	v_add_co_u32_e32 v84, vcc, s14, v78
	global_load_dwordx4 a[96:99], v[110:111], off
	global_load_dwordx4 a[104:107], v[110:111], off offset:1024
	global_load_dwordx4 a[108:111], v[58:59], off offset:1024
	global_load_dwordx4 a[116:119], v[58:59], off offset:2048
	global_load_dwordx4 a[112:115], v[110:111], off offset:2048
	global_load_dwordx4 a[120:123], v[110:111], off offset:3072
	global_load_dwordx4 a[100:103], v[112:113], off offset:-4096
	global_load_dwordx4 v[62:65], v[112:113], off
	global_load_dwordx4 a[124:127], v[58:59], off offset:3072
	s_nop 0
	global_load_dwordx4 v[58:61], v[114:115], off
	v_addc_co_u32_e32 v85, vcc, 0, v79, vcc
	v_add_co_u32_e32 v82, vcc, s15, v78
	s_add_i32 s8, s11, 0xa000
	s_nop 0
	v_addc_co_u32_e32 v83, vcc, 0, v79, vcc
	global_load_dwordx4 v[110:113], v[82:83], off offset:2048
	global_load_dwordx4 v[106:109], v[84:85], off offset:2048
	s_waitcnt vmcnt(39)
	ds_write_b128 v199, v[90:93] offset:12288
	s_waitcnt vmcnt(37)
	ds_write_b128 v199, v[94:97] offset:13312
	s_waitcnt vmcnt(36)
	ds_write_b128 v199, v[98:101] offset:14336
	s_waitcnt vmcnt(35)
	ds_write_b128 v199, v[102:105] offset:15360
	global_load_dwordx4 a[128:131], v[78:79], off
	global_load_dwordx4 a[132:135], v[84:85], off offset:-4096
	global_load_dwordx4 a[136:139], v[78:79], off offset:1024
	global_load_dwordx4 a[144:147], v[78:79], off offset:2048
	global_load_dwordx4 v[102:105], v[82:83], off offset:3072
	global_load_dwordx4 v[98:101], v[84:85], off offset:3072
	s_and_b32 s8, s8, 0xe000
	v_add_co_u32_e32 v80, vcc, s16, v78
	s_lshl_b32 s8, s8, 1
	s_nop 0
	v_addc_co_u32_e32 v81, vcc, 0, v79, vcc
	v_lshl_add_u64 v[122:123], v[74:75], 0, s[8:9]
	v_add_co_u32_e32 v124, vcc, s14, v122
	s_add_i32 s8, s11, 0xc000
	s_nop 0
	v_addc_co_u32_e32 v125, vcc, 0, v123, vcc
	v_add_co_u32_e32 v126, vcc, s15, v122
	s_and_b32 s8, s8, 0xc000
	s_nop 0
	v_addc_co_u32_e32 v127, vcc, 0, v123, vcc
	global_load_dwordx4 v[70:73], v[124:125], off offset:1024
	global_load_dwordx4 v[114:117], v[124:125], off offset:2048
	global_load_dwordx4 v[66:69], v[126:127], off offset:1024
	global_load_dwordx4 v[118:121], v[126:127], off offset:2048
	global_load_dwordx4 a[148:151], v[80:81], off offset:2048
	global_load_dwordx4 a[156:159], v[80:81], off offset:3072
	global_load_dwordx4 v[132:135], v[126:127], off offset:3072
	global_load_dwordx4 v[136:139], v[124:125], off offset:3072
	global_load_dwordx4 a[140:143], v[80:81], off offset:1024
	global_load_dwordx4 a[152:155], v[78:79], off offset:3072
	s_nop 0
	global_load_dwordx4 v[78:81], v[84:85], off
	global_load_dwordx4 v[86:89], v[84:85], off offset:1024
	s_lshl_b32 s8, s8, 1
	v_lshl_add_u64 v[164:165], v[74:75], 0, s[8:9]
	v_add_co_u32_e32 v176, vcc, s14, v164
	s_add_i32 s11, s11, 0xe000
	s_nop 0
	v_addc_co_u32_e32 v177, vcc, 0, v165, vcc
	v_add_co_u32_e32 v184, vcc, s15, v164
	s_and_b32 s8, s11, 0xe000
	s_nop 0
	v_addc_co_u32_e32 v185, vcc, 0, v165, vcc
	global_load_dwordx4 v[140:143], v[184:185], off offset:2048
	global_load_dwordx4 v[144:147], v[176:177], off offset:2048
	global_load_dwordx4 v[148:151], v[176:177], off offset:3072
	global_load_dwordx4 v[152:155], v[184:185], off offset:3072
	s_lshl_b32 s8, s8, 1
	v_lshl_add_u64 v[186:187], v[74:75], 0, s[8:9]
	v_add_co_u32_e32 v188, vcc, s14, v186
	v_and_or_b32 v74, v76, 16, v200
	s_nop 0
	v_addc_co_u32_e32 v189, vcc, 0, v187, vcc
	v_add_co_u32_e32 v190, vcc, s15, v186
	v_lshlrev_b32_e32 v129, 2, v74
	s_nop 0
	v_addc_co_u32_e32 v191, vcc, 0, v187, vcc
	global_load_dwordx4 v[94:97], v[188:189], off offset:1024
	global_load_dwordx4 v[156:159], v[188:189], off offset:2048
	global_load_dwordx4 v[90:93], v[190:191], off offset:1024
	global_load_dwordx4 v[160:163], v[190:191], off offset:2048
	global_load_dwordx4 v[172:175], v[188:189], off offset:3072
	global_load_dwordx4 v[180:183], v[190:191], off offset:3072
	s_waitcnt lgkmcnt(0)
	global_load_dword v131, v129, s[6:7]
	global_load_dwordx4 v[74:77], v[82:83], off
	s_nop 0
	global_load_dwordx4 v[82:85], v[82:83], off offset:1024
	s_waitcnt vmcnt(32)
	ds_write_b128 v199, v[110:113] offset:16384
	s_waitcnt vmcnt(31)
	ds_write_b128 v199, v[106:109] offset:17408
	v_lshlrev_b32_e32 v106, 7, v130
	v_or3_b32 v202, v106, v128, v179
	v_lshlrev_b32_e32 v106, 9, v201
	v_or_b32_e32 v107, 32, v129
	v_or3_b32 v106, v106, s10, v202
	global_load_dword v178, v129, s[6:7] offset:128
	global_load_dword v192, v107, s[6:7] offset:128
	global_load_dword v193, v129, s[6:7] offset:32
	v_ashrrev_i32_e32 v107, 31, v106
	v_lshl_add_u64 v[128:129], v[106:107], 2, s[4:5]
	global_load_dword v171, v[128:129], off
	s_waitcnt vmcnt(30)
	ds_write_b128 v199, v[102:105] offset:18432
	s_waitcnt vmcnt(29)
	ds_write_b128 v199, v[98:101] offset:19456
	v_add_co_u32_e32 v98, vcc, s16, v122
	s_mov_b32 s14, 0x45000000
	s_nop 0
	v_addc_co_u32_e32 v99, vcc, 0, v123, vcc
	global_load_dwordx4 a[160:163], v[122:123], off
	global_load_dwordx4 a[168:171], v[122:123], off offset:1024
	global_load_dwordx4 a[172:175], v[98:99], off offset:1024
	global_load_dwordx4 a[180:183], v[98:99], off offset:2048
	global_load_dwordx4 a[176:179], v[122:123], off offset:2048
	global_load_dwordx4 a[184:187], v[122:123], off offset:3072
	global_load_dword v170, v[128:129], off offset:64
	global_load_dwordx4 a[164:167], v[124:125], off offset:-4096
	global_load_dwordx4 v[102:105], v[124:125], off
	global_load_dwordx4 a[188:191], v[98:99], off offset:3072
	s_nop 0
	global_load_dwordx4 v[98:101], v[126:127], off
	s_waitcnt vmcnt(36)
	ds_write_b128 v199, v[118:121] offset:20480
	ds_write_b128 v199, v[114:117] offset:21504
	global_load_dword v169, v[128:129], off offset:128
	v_add_co_u32_e32 v106, vcc, s16, v164
	s_waitcnt vmcnt(34)
	ds_write_b128 v199, v[132:135] offset:22528
	s_waitcnt vmcnt(33)
	ds_write_b128 v199, v[136:139] offset:23552
	v_addc_co_u32_e32 v107, vcc, 0, v165, vcc
	global_load_dwordx4 a[192:195], v[164:165], off
	global_load_dwordx4 a[196:199], v[176:177], off offset:-4096
	global_load_dwordx4 a[200:203], v[164:165], off offset:1024
	global_load_dwordx4 a[208:211], v[164:165], off offset:2048
	global_load_dwordx4 a[212:215], v[106:107], off offset:2048
	global_load_dwordx4 a[220:223], v[106:107], off offset:3072
	global_load_dwordx4 a[204:207], v[106:107], off offset:1024
	global_load_dwordx4 a[216:219], v[164:165], off offset:3072
	global_load_dwordx4 v[110:113], v[176:177], off
	global_load_dwordx4 v[118:121], v[176:177], off offset:1024
	s_nop 0
	global_load_dwordx4 v[106:109], v[184:185], off
	global_load_dwordx4 v[114:117], v[184:185], off offset:1024
	global_load_dword v168, v[128:129], off offset:192
	v_add_co_u32_e32 v122, vcc, s16, v186
	v_and_b32_e32 v133, 32, v0
	s_nop 0
	v_addc_co_u32_e32 v123, vcc, 0, v187, vcc
	s_waitcnt vmcnt(41)
	ds_write_b128 v199, v[140:143] offset:24576
	s_waitcnt vmcnt(40)
	ds_write_b128 v199, v[144:147] offset:25600
	s_waitcnt vmcnt(38)
	ds_write_b128 v199, v[152:155] offset:26624
	ds_write_b128 v199, v[148:151] offset:27648
	global_load_dwordx4 a[224:227], v[186:187], off
	global_load_dwordx4 a[232:235], v[186:187], off offset:1024
	global_load_dwordx4 a[236:239], v[122:123], off offset:1024
	global_load_dwordx4 a[244:247], v[122:123], off offset:2048
	global_load_dwordx4 a[240:243], v[186:187], off offset:2048
	global_load_dwordx4 a[248:251], v[186:187], off offset:3072
	global_load_dwordx4 a[228:231], v[188:189], off offset:-4096
	global_load_dwordx4 v[126:129], v[188:189], off
	global_load_dwordx4 a[252:255], v[122:123], off offset:3072
	s_nop 0
	global_load_dwordx4 v[122:125], v[190:191], off
	v_lshlrev_b32_e32 v132, 2, v201
	v_lshl_or_b32 v130, v130, 6, v133
	v_lshrrev_b32_e32 v139, 1, v0
	v_and_b32_e32 v203, 24, v139
	s_waitcnt vmcnt(44)
	ds_write_b128 v199, v[160:163] offset:28672
	ds_write_b128 v199, v[156:159] offset:29696
	s_waitcnt vmcnt(42)
	ds_write_b128 v199, v[180:183] offset:30720
	ds_write_b128 v199, v[172:175] offset:31744
	s_waitcnt vmcnt(10) lgkmcnt(0)
	v_lshrrev_b32_e32 v222, 2, v131
	v_and_or_b32 v222, v222, 8, v132
	v_mul_u32_u24_e32 v222, 0x110, v222
	v_and_or_b32 v223, v131, 31, v130
	v_add_lshl_u32 v223, v223, v222, 1
	v_or_b32_e32 v204, 0x20000, v223
	v_lshrrev_b32_e32 v222, 2, v178
	v_and_or_b32 v222, v222, 8, v132
	v_mul_u32_u24_e32 v222, 0x110, v222
	v_and_or_b32 v223, v178, 31, v130
	v_add_lshl_u32 v223, v223, v222, 1
	v_or_b32_e32 v205, 0x20000, v223
	v_lshrrev_b32_e32 v222, 2, v193
	v_and_or_b32 v222, v222, 8, v132
	v_mul_u32_u24_e32 v222, 0x110, v222
	v_and_or_b32 v223, v193, 31, v130
	v_add_lshl_u32 v223, v223, v222, 1
	v_or_b32_e32 v206, 0x20000, v223
	v_lshrrev_b32_e32 v222, 2, v192
	v_and_or_b32 v222, v222, 8, v132
	v_mul_u32_u24_e32 v222, 0x110, v222
	v_and_or_b32 v223, v192, 31, v130
	v_add_lshl_u32 v223, v223, v222, 1
	v_or_b32_e32 v207, 0x20000, v223
	s_movk_i32 s43, 0x110
	v_mad_u32_u24 v224, v179, s43, v203
	v_mov_b32_e32 v225, 0x20000
	v_lshl_or_b32 v224, v224, 1, v225
	s_lshl_b32 s43, s3, 1
	s_add_u32 s52, s43, 0
	s_and_b32 s52, s52, 7
	s_lshl_b32 s52, s52, 6
	s_nop 0
	v_add_u32_e32 v208, s52, v224
	s_add_u32 s52, s43, 1
	s_and_b32 s52, s52, 7
	s_lshl_b32 s52, s52, 6
	s_sub_u32 s52, s52, 64
	s_nop 0
	v_add_u32_e32 v209, s52, v224
	s_add_u32 s52, s43, 2
	s_and_b32 s52, s52, 7
	s_lshl_b32 s52, s52, 6
	s_nop 0
	v_add_u32_e32 v211, s52, v224
	s_add_u32 s52, s43, 3
	s_and_b32 s52, s52, 7
	s_lshl_b32 s52, s52, 6
	s_nop 0
	v_add_u32_e32 v212, s52, v224
	s_add_u32 s52, s43, 4
	s_and_b32 s52, s52, 7
	s_lshl_b32 s52, s52, 6
	s_nop 0
	v_add_u32_e32 v213, s52, v224
	s_add_u32 s52, s43, 5
	s_and_b32 s52, s52, 7
	s_lshl_b32 s52, s52, 6
	s_nop 0
	v_add_u32_e32 v214, s52, v224
	s_add_u32 s52, s43, 6
	s_and_b32 s52, s52, 7
	s_lshl_b32 s52, s52, 6
	s_nop 0
	v_add_u32_e32 v215, s52, v224
	s_add_u32 s52, s43, 7
	s_and_b32 s52, s52, 7
	s_lshl_b32 s52, s52, 6
	s_nop 0
	v_add_u32_e32 v216, s52, v224
	v_and_b32_e32 v225, 8, v0
	v_cmp_eq_u32_e32 vcc, 0, v225
	v_mov_b32_e32 v225, 0xeeeeeeee
	s_nop 1
	v_cndmask_b32_e32 v210, v225, v196, vcc
	v_and_b32_e32 v225, 47, v0
	v_cmp_eq_u32_e64 s[4:5], 0, v225
	v_lshlrev_b32_e32 v225, 4, v167
	v_lshlrev_b32_e32 v226, 3, v201
	s_mov_b32 s52, 0x24400
	v_or3_b32 v218, v225, v226, s52
	s_load_dwordx2 s[6:7], s[0:1], 0x18
	s_lshl_b32 s11, s2, 9
	s_mov_b64 s[22:23], 0
	s_mov_b32 s29, 0
	s_mov_b32 s30, 0
	v_mov_b32_e32 v221, 0
	s_mov_b32 s40, 0x3a000000
	s_mov_b32 s41, 0x34800000
	s_mov_b32 s42, 0x45000000
	v_mov_b32_e32 v217, 0x24480
	v_mov_b64_e32 v[230:231], 0
	v_mov_b64_e32 v[232:233], 0
	v_mov_b64_e32 v[234:235], 0
	v_mov_b64_e32 v[236:237], 0
	v_mov_b64_e32 v[238:239], 0
	v_mov_b64_e32 v[240:241], 0
	v_mov_b64_e32 v[242:243], 0
	v_mov_b64_e32 v[244:245], 0
	ds_write_b128 v217, v[230:233]
	v_mov_b32_e32 v178, 0
	v_fma_mixlo_f16 v131, v178, v238, v171
	v_fma_mixlo_f16 v139, v178, v238, v170
	v_fma_mixlo_f16 v147, v178, v238, v169
	v_fma_mixlo_f16 v155, v178, v238, v168
	v_fma_f32 v130, v178, v238, v171
	v_fma_f32 v138, v178, v238, v170
	v_fma_f32 v146, v178, v238, v169
	v_fma_f32 v154, v178, v238, v168
	v_fma_mix_f32 v130, v130, 1.0, -v131 op_sel_hi:[0,0,1]
	v_fma_mix_f32 v138, v138, 1.0, -v139 op_sel_hi:[0,0,1]
	v_fma_mix_f32 v146, v146, 1.0, -v147 op_sel_hi:[0,0,1]
	v_fma_mix_f32 v154, v154, 1.0, -v155 op_sel_hi:[0,0,1]
	v_fma_mixlo_f16 v133, v130, s42, 0
	v_fma_mixlo_f16 v141, v138, s42, 0
	v_fma_mixlo_f16 v149, v146, s42, 0
	v_fma_mixlo_f16 v157, v154, s42, 0
	v_fma_mix_f32 v130, v130, s42, -v133 op_sel_hi:[0,0,1]
	v_fma_mix_f32 v138, v138, s42, -v141 op_sel_hi:[0,0,1]
	v_fma_mix_f32 v146, v146, s42, -v149 op_sel_hi:[0,0,1]
	v_fma_mix_f32 v154, v154, s42, -v157 op_sel_hi:[0,0,1]
	v_fma_mixlo_f16 v132, v130, s42, 0
	v_fma_mixlo_f16 v140, v138, s42, 0
	v_fma_mixlo_f16 v148, v146, s42, 0
	v_fma_mixlo_f16 v156, v154, s42, 0
	ds_write_b16 v204, v131
	ds_write_b16 v205, v139
	ds_write_b16 v206, v147
	ds_write_b16 v207, v155
	ds_write_b16 v204, v133 offset:544
	ds_write_b16 v205, v141 offset:544
	ds_write_b16 v206, v149 offset:544
	ds_write_b16 v207, v157 offset:544
	ds_write_b16 v204, v132 offset:1088
	ds_write_b16 v205, v140 offset:1088
	ds_write_b16 v206, v148 offset:1088
	ds_write_b16 v207, v156 offset:1088
	s_waitcnt lgkmcnt(0)
	s_barrier
	ds_read_b128 v[130:133], v208
	ds_read_b128 v[134:137], v209 offset:64
	ds_read_b128 v[138:141], v211
	ds_read_b128 v[142:145], v212
	ds_read_b128 v[146:149], v213
	ds_read_b128 v[150:153], v214
	ds_read_b128 v[154:157], v215
	ds_read_b128 v[158:161], v216
	s_waitcnt vmcnt(0)
	ds_read_b128 v[180:183], v199 offset:0
	ds_read_b128 v[184:187], v199 offset:1024
	ds_read_b128 v[188:191], v199 offset:4096
	ds_read_b128 v[192:195], v199 offset:5120
	ds_read_b128 v[222:225], v199 offset:8192
	s_waitcnt lgkmcnt(6)
	ds_read_b128 v[226:229], v199 offset:9216
	v_smfmac_f32_16x16x64_f16 v[230:233], v[130:133], a[0:7], v210
	v_smfmac_f32_16x16x64_f16 v[234:237], v[130:133], v[18:25], v210
	v_smfmac_f32_16x16x64_f16 v[230:233], v[134:137], a[40:47], v210
	v_smfmac_f32_16x16x64_f16 v[234:237], v[134:137], v[34:41], v210
	v_smfmac_f32_16x16x64_f16 v[230:233], v[138:141], a[64:71], v210
	v_smfmac_f32_16x16x64_f16 v[234:237], v[138:141], v[42:49], v210
	v_smfmac_f32_16x16x64_f16 v[230:233], v[142:145], a[96:103], v210
	v_smfmac_f32_16x16x64_f16 v[234:237], v[142:145], v[58:65], v210
	v_smfmac_f32_16x16x64_f16 v[230:233], v[146:149], a[128:135], v210
	v_smfmac_f32_16x16x64_f16 v[234:237], v[146:149], v[74:81], v210
	v_smfmac_f32_16x16x64_f16 v[230:233], v[150:153], a[160:167], v210
	v_smfmac_f32_16x16x64_f16 v[234:237], v[150:153], v[98:105], v210
	v_smfmac_f32_16x16x64_f16 v[230:233], v[154:157], a[192:199], v210
	v_smfmac_f32_16x16x64_f16 v[234:237], v[154:157], v[106:113], v210
	s_waitcnt lgkmcnt(6)
	v_smfmac_f32_16x16x64_f16 v[230:233], v[158:161], a[224:231], v210
	v_smfmac_f32_16x16x64_f16 v[234:237], v[158:161], v[122:129], v210
	v_smfmac_f32_16x16x64_f16 v[238:241], v[130:133], a[16:23], v210
	s_waitcnt lgkmcnt(4)
	v_smfmac_f32_16x16x64_f16 v[242:245], v[130:133], v[180:187], v210
	ds_read_b128 v[180:183], v199 offset:12288
	ds_read_b128 v[184:187], v199 offset:13312
	v_smfmac_f32_16x16x64_f16 v[238:241], v[134:137], a[48:55], v210
	v_fmac_f32_e32 v230, s40, v231
	s_waitcnt lgkmcnt(4)
	v_smfmac_f32_16x16x64_f16 v[242:245], v[134:137], v[188:195], v210
	ds_read_b128 v[188:191], v199 offset:16384
	ds_read_b128 v[192:195], v199 offset:17408
	v_fmac_f32_e32 v234, s40, v235
	v_smfmac_f32_16x16x64_f16 v[238:241], v[138:141], a[80:87], v210
	v_fmac_f32_e32 v230, s41, v232
	s_waitcnt lgkmcnt(4)
	v_smfmac_f32_16x16x64_f16 v[242:245], v[138:141], v[222:229], v210
	ds_read_b128 v[222:225], v199 offset:20480
	ds_read_b128 v[226:229], v199 offset:21504
	v_fmac_f32_e32 v234, s41, v236
	v_smfmac_f32_16x16x64_f16 v[238:241], v[142:145], a[112:119], v210
	s_nop 0
	v_permlane32_swap_b32_e32 v230, v234
	s_waitcnt lgkmcnt(4)
	v_smfmac_f32_16x16x64_f16 v[242:245], v[142:145], v[180:187], v210
	ds_read_b128 v[180:183], v199 offset:24576
	ds_read_b128 v[184:187], v199 offset:25600
	v_add_f32_e32 v173, v230, v234
	v_smfmac_f32_16x16x64_f16 v[238:241], v[146:149], a[144:151], v210
	ds_read_b128 v[230:233], v217
	s_waitcnt lgkmcnt(5)
	v_smfmac_f32_16x16x64_f16 v[242:245], v[146:149], v[188:195], v210
	ds_read_b128 v[188:191], v199 offset:28672
	ds_read_b128 v[192:195], v199 offset:29696
	ds_read_b128 v[234:237], v217
	v_smfmac_f32_16x16x64_f16 v[238:241], v[150:153], a[176:183], v210
	s_waitcnt lgkmcnt(6)
	v_smfmac_f32_16x16x64_f16 v[242:245], v[150:153], v[222:229], v210
	ds_read_b128 v[222:225], v199 offset:2048
	ds_read_b128 v[226:229], v199 offset:3072
	v_smfmac_f32_16x16x64_f16 v[238:241], v[154:157], a[208:215], v210
	s_waitcnt lgkmcnt(6)
	v_smfmac_f32_16x16x64_f16 v[242:245], v[154:157], v[180:187], v210
	ds_read_b128 v[180:183], v199 offset:6144
	ds_read_b128 v[184:187], v199 offset:7168
	v_smfmac_f32_16x16x64_f16 v[238:241], v[158:161], a[240:247], v210
	s_waitcnt lgkmcnt(5)
	v_smfmac_f32_16x16x64_f16 v[242:245], v[158:161], v[188:195], v210
	ds_read_b128 v[188:191], v199 offset:10240
	ds_read_b128 v[192:195], v199 offset:11264
	v_smfmac_f32_16x16x64_f16 v[230:233], v[130:133], a[8:15], v210
	s_waitcnt lgkmcnt(6)
	v_smfmac_f32_16x16x64_f16 v[234:237], v[130:133], v[2:9], v210
	v_smfmac_f32_16x16x64_f16 v[230:233], v[134:137], a[32:39], v210
	v_fmac_f32_e32 v238, s40, v239
	v_smfmac_f32_16x16x64_f16 v[234:237], v[134:137], v[10:17], v210
	v_fmac_f32_e32 v242, s40, v243
	v_smfmac_f32_16x16x64_f16 v[230:233], v[138:141], a[72:79], v210
	v_fmac_f32_e32 v238, s41, v240
	v_smfmac_f32_16x16x64_f16 v[234:237], v[138:141], v[50:57], v210
	v_fmac_f32_e32 v242, s41, v244
	v_smfmac_f32_16x16x64_f16 v[230:233], v[142:145], a[104:111], v210
	s_nop 0
	v_permlane32_swap_b32_e32 v238, v242
	v_smfmac_f32_16x16x64_f16 v[234:237], v[142:145], v[26:33], v210
	v_add_f32_e32 v175, v238, v242
	v_smfmac_f32_16x16x64_f16 v[230:233], v[146:149], a[136:143], v210
	ds_read_b128 v[238:241], v217
	v_smfmac_f32_16x16x64_f16 v[234:237], v[146:149], v[82:89], v210
	ds_read_b128 v[242:245], v217
	v_smfmac_f32_16x16x64_f16 v[230:233], v[150:153], a[168:175], v210
	v_smfmac_f32_16x16x64_f16 v[234:237], v[150:153], v[66:73], v210
	v_smfmac_f32_16x16x64_f16 v[230:233], v[154:157], a[200:207], v210
	v_smfmac_f32_16x16x64_f16 v[234:237], v[154:157], v[114:121], v210
	v_smfmac_f32_16x16x64_f16 v[230:233], v[158:161], a[232:239], v210
	v_smfmac_f32_16x16x64_f16 v[234:237], v[158:161], v[90:97], v210
	s_waitcnt lgkmcnt(1)
	v_smfmac_f32_16x16x64_f16 v[238:241], v[130:133], a[24:31], v210
	s_waitcnt lgkmcnt(0)
	v_smfmac_f32_16x16x64_f16 v[242:245], v[130:133], v[222:229], v210
	ds_read_b128 v[222:225], v199 offset:14336
	ds_read_b128 v[226:229], v199 offset:15360
	v_smfmac_f32_16x16x64_f16 v[238:241], v[134:137], a[56:63], v210
	v_fmac_f32_e32 v230, s40, v231
	v_smfmac_f32_16x16x64_f16 v[242:245], v[134:137], v[180:187], v210
	ds_read_b128 v[180:183], v199 offset:18432
	ds_read_b128 v[184:187], v199 offset:19456
	v_fmac_f32_e32 v234, s40, v235
	v_smfmac_f32_16x16x64_f16 v[238:241], v[138:141], a[88:95], v210
	v_fmac_f32_e32 v230, s41, v232
	v_smfmac_f32_16x16x64_f16 v[242:245], v[138:141], v[188:195], v210
	ds_read_b128 v[188:191], v199 offset:22528
	ds_read_b128 v[192:195], v199 offset:23552
	v_fmac_f32_e32 v234, s41, v236
	v_smfmac_f32_16x16x64_f16 v[238:241], v[142:145], a[120:127], v210
	s_nop 0
	v_permlane32_swap_b32_e32 v230, v234
	s_waitcnt lgkmcnt(4)
	v_smfmac_f32_16x16x64_f16 v[242:245], v[142:145], v[222:229], v210
	ds_read_b128 v[222:225], v199 offset:26624
	ds_read_b128 v[226:229], v199 offset:27648
	v_add_f32_e32 v172, v230, v234
	v_smfmac_f32_16x16x64_f16 v[238:241], v[146:149], a[152:159], v210
	ds_read_b128 v[230:233], v217
	s_waitcnt lgkmcnt(5)
	v_smfmac_f32_16x16x64_f16 v[242:245], v[146:149], v[180:187], v210
	ds_read_b128 v[180:183], v199 offset:30720
	ds_read_b128 v[184:187], v199 offset:31744
	ds_read_b128 v[234:237], v217
	v_smfmac_f32_16x16x64_f16 v[238:241], v[150:153], a[184:191], v210
	s_waitcnt lgkmcnt(6)
	v_smfmac_f32_16x16x64_f16 v[242:245], v[150:153], v[188:195], v210
	v_smfmac_f32_16x16x64_f16 v[238:241], v[154:157], a[216:223], v210
	s_waitcnt lgkmcnt(4)
	v_smfmac_f32_16x16x64_f16 v[242:245], v[154:157], v[222:229], v210
	v_smfmac_f32_16x16x64_f16 v[238:241], v[158:161], a[248:255], v210
	s_waitcnt lgkmcnt(1)
	v_smfmac_f32_16x16x64_f16 v[242:245], v[158:161], v[180:187], v210
	s_nop 5
	v_fmac_f32_e32 v238, s40, v239
	s_nop 0
	v_fmac_f32_e32 v242, s40, v243
	v_fmac_f32_e32 v238, s41, v240
	v_fmac_f32_e32 v242, s41, v244
	s_nop 1
	v_permlane32_swap_b32_e32 v238, v242
	v_add_f32_e32 v174, v238, v242
	s_mov_b32 s52, 0x3a83126f
	v_mov_b32_e32 v245, 0x358637bd
	v_fma_f32 v179, |v171|, s52, v245
	v_fma_f32 v196, |v170|, s52, v245
	v_fma_f32 v197, |v169|, s52, v245
	v_fma_f32 v198, |v168|, s52, v245
	v_rcp_f32_e32 v179, v179
	v_rcp_f32_e32 v196, v196
	v_rcp_f32_e32 v197, v197
	v_rcp_f32_e32 v198, v198
	v_mul_f32_e32 v238, v170, v196
	v_mul_f32_e32 v239, 0x3b000000, v172
	v_mul_f32_e32 v239, v239, v196
	v_mul_f32_e32 v130, v238, v238
	v_mul_f32_e32 v131, v239, v239
	v_mul_f32_e32 v238, v171, v179
	v_mul_f32_e32 v239, 0x3b000000, v173
	v_mul_f32_e32 v239, v239, v179
	v_fmac_f32_e32 v130, v238, v238
	v_fmac_f32_e32 v131, v239, v239
	v_mul_f32_e32 v238, v169, v197
	v_mul_f32_e32 v239, 0x3b000000, v175
	v_mul_f32_e32 v239, v239, v197
	v_fmac_f32_e32 v130, v238, v238
	v_fmac_f32_e32 v131, v239, v239
	v_mul_f32_e32 v238, v168, v198
	v_mul_f32_e32 v239, 0x3b000000, v174
	v_mul_f32_e32 v239, v239, v198
	v_fmac_f32_e32 v130, v238, v238
	v_fmac_f32_e32 v131, v239, v239
	s_nop 0
	v_add_f32_dpp v130, v130, v130 quad_perm:[1,0,3,2] row_mask:0xf bank_mask:0xf bound_ctrl:1
	v_add_f32_dpp v131, v131, v131 quad_perm:[1,0,3,2] row_mask:0xf bank_mask:0xf bound_ctrl:1
	s_nop 0
	v_add_f32_dpp v130, v130, v130 quad_perm:[2,3,0,1] row_mask:0xf bank_mask:0xf bound_ctrl:1
	v_add_f32_dpp v131, v131, v131 quad_perm:[2,3,0,1] row_mask:0xf bank_mask:0xf bound_ctrl:1
	s_nop 0
	v_add_f32_dpp v130, v130, v130 row_half_mirror row_mask:0xf bank_mask:0xf bound_ctrl:1
	v_add_f32_dpp v131, v131, v131 row_half_mirror row_mask:0xf bank_mask:0xf bound_ctrl:1
	s_nop 0
	v_add_f32_dpp v130, v130, v130 row_mirror row_mask:0xf bank_mask:0xf bound_ctrl:1
	v_add_f32_dpp v131, v131, v131 row_mirror row_mask:0xf bank_mask:0xf bound_ctrl:1
	v_mov_b32_e32 v240, v130
	v_mov_b32_e32 v241, v131
	s_nop 0
	v_permlane32_swap_b32_e32 v130, v240
	v_permlane32_swap_b32_e32 v131, v241
	v_add_f32_e32 v130, v130, v240
	v_add_f32_e32 v131, v131, v241
	v_add_u32_e32 v242, 0, v218
	v_lshlrev_b32_e32 v243, 3, v201
	v_or_b32_e32 v243, 0x24400, v243
	s_and_saveexec_b64 s[2:3], s[4:5]
	ds_write_b64 v242, v[130:131]
	s_or_b64 exec, exec, s[2:3]
	s_waitcnt lgkmcnt(0)
	s_barrier
	ds_read_b64 v[134:135], v243 offset:0
	ds_read_b64 v[138:139], v243 offset:16
	ds_read_b64 v[142:143], v243 offset:32
	ds_read_b64 v[146:147], v243 offset:48
	s_waitcnt lgkmcnt(2)
	v_add_f32_e32 v238, v134, v138
	s_waitcnt lgkmcnt(1)
	v_add_f32_e32 v238, v238, v142
	s_waitcnt lgkmcnt(0)
	v_add_f32_e32 v238, v238, v146
	v_add_f32_e32 v239, v135, v139
	v_add_f32_e32 v239, v239, v143
	v_add_f32_e32 v239, v239, v147
	v_mul_f32_e32 v238, 0x3b000000, v238
	v_max_f32_e32 v238, 0xda24260, v238
	v_sqrt_f32_e32 v238, v238
	v_mul_f32_e32 v239, 0x3b000000, v239
	v_max_f32_e32 v239, 0xda24260, v239
	v_sqrt_f32_e32 v239, v239
	s_nop 0
	v_mov_b32_e32 v220, v239
	v_rcp_f32_e32 v240, v239
	v_min_f32_e32 v241, v238, v239
	v_mul_f32_e32 v238, 0x3c23d70a, v238
	v_mul_f32_e32 v238, v238, v240
	s_mov_b32 s52, 0x3727c5ac
	v_cmp_ngt_f32_e32 vcc, s52, v241
	v_mov_b32_e32 v240, 0x358637bd
	s_nop 1
	v_cndmask_b32_e32 v219, v240, v238, vcc
	v_mul_f32_e32 v178, 0x3b000000, v219
	v_fma_mixlo_f16 v131, v178, v173, v171
	v_fma_mixlo_f16 v139, v178, v172, v170
	v_fma_mixlo_f16 v147, v178, v175, v169
	v_fma_mixlo_f16 v155, v178, v174, v168
	v_fma_f32 v130, v178, v173, v171
	v_fma_f32 v138, v178, v172, v170
	v_fma_f32 v146, v178, v175, v169
	v_fma_f32 v154, v178, v174, v168
	v_fma_mix_f32 v130, v130, 1.0, -v131 op_sel_hi:[0,0,1]
	v_fma_mix_f32 v138, v138, 1.0, -v139 op_sel_hi:[0,0,1]
	v_fma_mix_f32 v146, v146, 1.0, -v147 op_sel_hi:[0,0,1]
	v_fma_mix_f32 v154, v154, 1.0, -v155 op_sel_hi:[0,0,1]
	v_fma_mixlo_f16 v133, v130, s42, 0
	v_fma_mixlo_f16 v141, v138, s42, 0
	v_fma_mixlo_f16 v149, v146, s42, 0
	v_fma_mixlo_f16 v157, v154, s42, 0
	v_fma_mix_f32 v130, v130, s42, -v133 op_sel_hi:[0,0,1]
	v_fma_mix_f32 v138, v138, s42, -v141 op_sel_hi:[0,0,1]
	v_fma_mix_f32 v146, v146, s42, -v149 op_sel_hi:[0,0,1]
	v_fma_mix_f32 v154, v154, s42, -v157 op_sel_hi:[0,0,1]
	v_fma_mixlo_f16 v132, v130, s42, 0
	v_fma_mixlo_f16 v140, v138, s42, 0
	v_fma_mixlo_f16 v148, v146, s42, 0
	v_fma_mixlo_f16 v156, v154, s42, 0
	ds_write_b16 v204, v131 offset:8704
	ds_write_b16 v205, v139 offset:8704
	ds_write_b16 v206, v147 offset:8704
	ds_write_b16 v207, v155 offset:8704
	ds_write_b16 v204, v133 offset:9248
	ds_write_b16 v205, v141 offset:9248
	ds_write_b16 v206, v149 offset:9248
	ds_write_b16 v207, v157 offset:9248
	ds_write_b16 v204, v132 offset:9792
	ds_write_b16 v205, v140 offset:9792
	ds_write_b16 v206, v148 offset:9792
	ds_write_b16 v207, v156 offset:9792
	s_waitcnt lgkmcnt(0)
	s_barrier
	ds_read_b128 v[130:133], v208 offset:8704
	ds_read_b128 v[134:137], v209 offset:8768
	ds_read_b128 v[138:141], v211 offset:8704
	ds_read_b128 v[142:145], v212 offset:8704
	ds_read_b128 v[146:149], v213 offset:8704
	ds_read_b128 v[150:153], v214 offset:8704
	ds_read_b128 v[154:157], v215 offset:8704
	ds_read_b128 v[158:161], v216 offset:8704
	ds_read_b128 v[180:183], v199 offset:0
	ds_read_b128 v[184:187], v199 offset:1024
	ds_read_b128 v[188:191], v199 offset:4096
	ds_read_b128 v[192:195], v199 offset:5120
	ds_read_b128 v[222:225], v199 offset:8192
	s_waitcnt lgkmcnt(6)
	ds_read_b128 v[226:229], v199 offset:9216
	v_smfmac_f32_16x16x64_f16 v[230:233], v[130:133], a[0:7], v210
	ds_read_b128 v[238:241], v217
	v_smfmac_f32_16x16x64_f16 v[234:237], v[130:133], v[18:25], v210
	ds_read_b128 v[242:245], v217
	v_smfmac_f32_16x16x64_f16 v[230:233], v[134:137], a[40:47], v210
	v_smfmac_f32_16x16x64_f16 v[234:237], v[134:137], v[34:41], v210
	v_smfmac_f32_16x16x64_f16 v[230:233], v[138:141], a[64:71], v210
	v_smfmac_f32_16x16x64_f16 v[234:237], v[138:141], v[42:49], v210
	v_smfmac_f32_16x16x64_f16 v[230:233], v[142:145], a[96:103], v210
	v_smfmac_f32_16x16x64_f16 v[234:237], v[142:145], v[58:65], v210
	v_smfmac_f32_16x16x64_f16 v[230:233], v[146:149], a[128:135], v210
	v_smfmac_f32_16x16x64_f16 v[234:237], v[146:149], v[74:81], v210
	v_smfmac_f32_16x16x64_f16 v[230:233], v[150:153], a[160:167], v210
	v_smfmac_f32_16x16x64_f16 v[234:237], v[150:153], v[98:105], v210
	v_smfmac_f32_16x16x64_f16 v[230:233], v[154:157], a[192:199], v210
	v_smfmac_f32_16x16x64_f16 v[234:237], v[154:157], v[106:113], v210
	s_waitcnt lgkmcnt(8)
	v_smfmac_f32_16x16x64_f16 v[230:233], v[158:161], a[224:231], v210
	v_smfmac_f32_16x16x64_f16 v[234:237], v[158:161], v[122:129], v210
	s_waitcnt lgkmcnt(1)
	v_smfmac_f32_16x16x64_f16 v[238:241], v[130:133], a[16:23], v210
	s_waitcnt lgkmcnt(0)
	v_smfmac_f32_16x16x64_f16 v[242:245], v[130:133], v[180:187], v210
	ds_read_b128 v[180:183], v199 offset:12288
	ds_read_b128 v[184:187], v199 offset:13312
	v_smfmac_f32_16x16x64_f16 v[238:241], v[134:137], a[48:55], v210
	v_fmac_f32_e32 v230, s40, v231
	v_smfmac_f32_16x16x64_f16 v[242:245], v[134:137], v[188:195], v210
	ds_read_b128 v[188:191], v199 offset:16384
	ds_read_b128 v[192:195], v199 offset:17408
	v_fmac_f32_e32 v234, s40, v235
	v_smfmac_f32_16x16x64_f16 v[238:241], v[138:141], a[80:87], v210
	v_fmac_f32_e32 v230, s41, v232
	v_smfmac_f32_16x16x64_f16 v[242:245], v[138:141], v[222:229], v210
	ds_read_b128 v[222:225], v199 offset:20480
	ds_read_b128 v[226:229], v199 offset:21504
	v_fmac_f32_e32 v234, s41, v236
	v_smfmac_f32_16x16x64_f16 v[238:241], v[142:145], a[112:119], v210
	s_nop 0
	v_permlane32_swap_b32_e32 v230, v234
	s_waitcnt lgkmcnt(4)
	v_smfmac_f32_16x16x64_f16 v[242:245], v[142:145], v[180:187], v210
	ds_read_b128 v[180:183], v199 offset:24576
	ds_read_b128 v[184:187], v199 offset:25600
	v_add_f32_e32 v162, v230, v234
	v_smfmac_f32_16x16x64_f16 v[238:241], v[146:149], a[144:151], v210
	ds_read_b128 v[230:233], v217
	s_waitcnt lgkmcnt(5)
	v_smfmac_f32_16x16x64_f16 v[242:245], v[146:149], v[188:195], v210
	ds_read_b128 v[188:191], v199 offset:28672
	ds_read_b128 v[192:195], v199 offset:29696
	ds_read_b128 v[234:237], v217
	v_smfmac_f32_16x16x64_f16 v[238:241], v[150:153], a[176:183], v210
	s_waitcnt lgkmcnt(6)
	v_smfmac_f32_16x16x64_f16 v[242:245], v[150:153], v[222:229], v210
	ds_read_b128 v[222:225], v199 offset:2048
	ds_read_b128 v[226:229], v199 offset:3072
	v_smfmac_f32_16x16x64_f16 v[238:241], v[154:157], a[208:215], v210
	s_waitcnt lgkmcnt(6)
	v_smfmac_f32_16x16x64_f16 v[242:245], v[154:157], v[180:187], v210
	ds_read_b128 v[180:183], v199 offset:6144
	ds_read_b128 v[184:187], v199 offset:7168
	v_smfmac_f32_16x16x64_f16 v[238:241], v[158:161], a[240:247], v210
	s_waitcnt lgkmcnt(5)
	v_smfmac_f32_16x16x64_f16 v[242:245], v[158:161], v[188:195], v210
	ds_read_b128 v[188:191], v199 offset:10240
	ds_read_b128 v[192:195], v199 offset:11264
	v_smfmac_f32_16x16x64_f16 v[230:233], v[130:133], a[8:15], v210
	s_waitcnt lgkmcnt(6)
	v_smfmac_f32_16x16x64_f16 v[234:237], v[130:133], v[2:9], v210
	v_smfmac_f32_16x16x64_f16 v[230:233], v[134:137], a[32:39], v210
	v_fmac_f32_e32 v238, s40, v239
	v_smfmac_f32_16x16x64_f16 v[234:237], v[134:137], v[10:17], v210
	v_fmac_f32_e32 v242, s40, v243
	v_smfmac_f32_16x16x64_f16 v[230:233], v[138:141], a[72:79], v210
	v_fmac_f32_e32 v238, s41, v240
	v_smfmac_f32_16x16x64_f16 v[234:237], v[138:141], v[50:57], v210
	v_fmac_f32_e32 v242, s41, v244
	v_smfmac_f32_16x16x64_f16 v[230:233], v[142:145], a[104:111], v210
	s_nop 0
	v_permlane32_swap_b32_e32 v238, v242
	v_smfmac_f32_16x16x64_f16 v[234:237], v[142:145], v[26:33], v210
	v_add_f32_e32 v164, v238, v242
	v_smfmac_f32_16x16x64_f16 v[230:233], v[146:149], a[136:143], v210
	ds_read_b128 v[238:241], v217
	v_smfmac_f32_16x16x64_f16 v[234:237], v[146:149], v[82:89], v210
	ds_read_b128 v[242:245], v217
	v_smfmac_f32_16x16x64_f16 v[230:233], v[150:153], a[168:175], v210
	v_smfmac_f32_16x16x64_f16 v[234:237], v[150:153], v[66:73], v210
	v_smfmac_f32_16x16x64_f16 v[230:233], v[154:157], a[200:207], v210
	v_smfmac_f32_16x16x64_f16 v[234:237], v[154:157], v[114:121], v210
	v_smfmac_f32_16x16x64_f16 v[230:233], v[158:161], a[232:239], v210
	v_smfmac_f32_16x16x64_f16 v[234:237], v[158:161], v[90:97], v210
	s_waitcnt lgkmcnt(1)
	v_smfmac_f32_16x16x64_f16 v[238:241], v[130:133], a[24:31], v210
	s_waitcnt lgkmcnt(0)
	v_smfmac_f32_16x16x64_f16 v[242:245], v[130:133], v[222:229], v210
	ds_read_b128 v[222:225], v199 offset:14336
	ds_read_b128 v[226:229], v199 offset:15360
	v_smfmac_f32_16x16x64_f16 v[238:241], v[134:137], a[56:63], v210
	v_fmac_f32_e32 v230, s40, v231
	v_smfmac_f32_16x16x64_f16 v[242:245], v[134:137], v[180:187], v210
	ds_read_b128 v[180:183], v199 offset:18432
	ds_read_b128 v[184:187], v199 offset:19456
	v_fmac_f32_e32 v234, s40, v235
	v_smfmac_f32_16x16x64_f16 v[238:241], v[138:141], a[88:95], v210
	v_fmac_f32_e32 v230, s41, v232
	v_smfmac_f32_16x16x64_f16 v[242:245], v[138:141], v[188:195], v210
	ds_read_b128 v[188:191], v199 offset:22528
	ds_read_b128 v[192:195], v199 offset:23552
	v_fmac_f32_e32 v234, s41, v236
	v_smfmac_f32_16x16x64_f16 v[238:241], v[142:145], a[120:127], v210
	s_nop 0
	v_permlane32_swap_b32_e32 v230, v234
	s_waitcnt lgkmcnt(4)
	v_smfmac_f32_16x16x64_f16 v[242:245], v[142:145], v[222:229], v210
	ds_read_b128 v[222:225], v199 offset:26624
	ds_read_b128 v[226:229], v199 offset:27648
	v_add_f32_e32 v163, v230, v234
	v_smfmac_f32_16x16x64_f16 v[238:241], v[146:149], a[152:159], v210
	ds_read_b128 v[230:233], v217
	s_waitcnt lgkmcnt(5)
	v_smfmac_f32_16x16x64_f16 v[242:245], v[146:149], v[180:187], v210
	ds_read_b128 v[180:183], v199 offset:30720
	ds_read_b128 v[184:187], v199 offset:31744
	ds_read_b128 v[234:237], v217
	v_smfmac_f32_16x16x64_f16 v[238:241], v[150:153], a[184:191], v210
	s_waitcnt lgkmcnt(6)
	v_smfmac_f32_16x16x64_f16 v[242:245], v[150:153], v[188:195], v210
	v_smfmac_f32_16x16x64_f16 v[238:241], v[154:157], a[216:223], v210
	s_waitcnt lgkmcnt(4)
	v_smfmac_f32_16x16x64_f16 v[242:245], v[154:157], v[222:229], v210
	v_smfmac_f32_16x16x64_f16 v[238:241], v[158:161], a[248:255], v210
	s_waitcnt lgkmcnt(1)
	v_smfmac_f32_16x16x64_f16 v[242:245], v[158:161], v[180:187], v210
	s_nop 5
	v_fmac_f32_e32 v238, s40, v239
	s_nop 0
	v_fmac_f32_e32 v242, s40, v243
	v_fmac_f32_e32 v238, s41, v240
	v_fmac_f32_e32 v242, s41, v244
	s_nop 1
	v_permlane32_swap_b32_e32 v238, v242
	v_add_f32_e32 v165, v238, v242
	v_sub_f32_e32 v238, v163, v172
	v_mul_f32_e32 v238, 0x3b000000, v238
	v_mul_f32_e32 v238, v238, v196
	v_mul_f32_e32 v130, v238, v238
	v_sub_f32_e32 v238, v162, v173
	v_mul_f32_e32 v238, 0x3b000000, v238
	v_mul_f32_e32 v238, v238, v179
	v_fmac_f32_e32 v130, v238, v238
	v_sub_f32_e32 v238, v164, v175
	v_mul_f32_e32 v238, 0x3b000000, v238
	v_mul_f32_e32 v238, v238, v197
	v_fmac_f32_e32 v130, v238, v238
	v_sub_f32_e32 v238, v165, v174
	v_mul_f32_e32 v238, 0x3b000000, v238
	v_mul_f32_e32 v238, v238, v198
	v_fmac_f32_e32 v130, v238, v238
	s_nop 1
	v_add_f32_dpp v130, v130, v130 quad_perm:[1,0,3,2] row_mask:0xf bank_mask:0xf bound_ctrl:1
	s_nop 1
	v_add_f32_dpp v130, v130, v130 quad_perm:[2,3,0,1] row_mask:0xf bank_mask:0xf bound_ctrl:1
	s_nop 1
	v_add_f32_dpp v130, v130, v130 row_half_mirror row_mask:0xf bank_mask:0xf bound_ctrl:1
	s_nop 1
	v_add_f32_dpp v130, v130, v130 row_mirror row_mask:0xf bank_mask:0xf bound_ctrl:1
	v_mov_b32_e32 v240, v130
	s_nop 1
	v_permlane32_swap_b32_e32 v130, v240
	v_add_f32_e32 v130, v130, v240
	v_add_u32_e32 v242, 64, v218
	v_lshlrev_b32_e32 v243, 3, v201
	v_or_b32_e32 v243, 0x24440, v243
	s_and_saveexec_b64 s[2:3], s[4:5]
	ds_write_b32 v242, v130
	s_or_b64 exec, exec, s[2:3]
	s_waitcnt lgkmcnt(0)
	s_barrier
	ds_read2_b32 v[134:135], v243 offset1:4
	ds_read2_b32 v[136:137], v243 offset0:8 offset1:12
	s_waitcnt lgkmcnt(1)
	v_add_f32_e32 v238, v134, v135
	s_waitcnt lgkmcnt(0)
	v_add_f32_e32 v238, v238, v136
	v_add_f32_e32 v238, v238, v137
	v_mul_f32_e32 v238, 0x3b000000, v238
	v_max_f32_e32 v238, 0xda24260, v238
	v_rcp_f32_e32 v240, v219
	v_sqrt_f32_e32 v238, v238
	s_nop 0
	v_mul_f32_e32 v238, v240, v238
	v_max_f32_e32 v241, v220, v238
	v_mul_f32_e32 v242, 0x3a83126f, v219
	v_max_f32_e32 v242, 0x358637bd, v242
	v_max_f32_e32 v243, 0x26901d7d, v241
	v_rcp_f32_e32 v243, v243
	s_nop 0
	v_mul_f32_e32 v243, 0x3c23d70a, v243
	v_log_f32_e32 v243, v243
	s_nop 0
	v_mul_f32_e32 v243, 0x3e4ccccd, v243
	v_exp_f32_e32 v243, v243
	s_mov_b32 s52, 0x26901d7d
	v_cmp_ge_f32_e32 vcc, s52, v241
	s_nop 1
	v_cndmask_b32_e32 v243, v243, v242, vcc
	v_mul_f32_e32 v242, 0x42c80000, v219
	v_min3_f32 v1, v242, v243, 1.0
